# dense q|k|v copy (pitch 1536 B) written by hand-written in-proj epilogue, attention reads it; static attention all in scan phase; R2+M2 rewrites
# speedup vs baseline: 1.0252x; 1.0111x over previous
; __device__ __forceinline__ unsigned cvt_pk_bf16(float lo, float hi) { unsigned r; asm volatile("v_cvt_pk_bf16_f32 %0, %1, %2" : "=v"(r) : "v"(lo), "v"(hi)); return r; }
;     __device__ __forceinline__ void operator()(const f32x4 (&acc)[2][2][4][2], const Unit& u, int wr, int wc, int fr, int fq) const {
;         const int row0 = u.pm * BM + wr * 64 + fr; int colt = u.pn * BM; bf16_t* base = O;
;         float sc = 1.f; if (split_cols) { const int t = colt / split_cols; base += (size_t)t * split_stride; colt -= t * split_cols; if (t == 0) sc = scale0; }
;         const int col0 = colt + wc * 32 + 8 * fq, bcol0 = u.pn * BM + wc * 32 + 8 * fq;
;         f32x4 bv[2][2];
; #pragma unroll
;         for (int bj = 0; bj < 2; ++bj)
; #pragma unroll
;             for (int n = 0; n < 2; ++n) bv[bj][n] = bias ? *(const f32x4*)(bias + bcol0 + bj * HALF + 4 * n) : (f32x4){0.f, 0.f, 0.f, 0.f};
; #pragma unroll
;         for (int ai = 0; ai < 2; ++ai)
; #pragma unroll
;             for (int m = 0; m < 4; ++m) { bf16_t* rowp = base + (size_t)(row0 + ai * HALF + m * 16) * ldc + col0;
; #pragma unroll
;                 for (int bj = 0; bj < 2; ++bj) { f32x4 v0 = acc[ai][bj][m][0] + bv[bj][0], v1 = acc[ai][bj][m][1] + bv[bj][1];
;                     if (ACT == 1) { f32x2 a = gelu_pk((f32x2){v0[0], v0[1]}), b = gelu_pk((f32x2){v0[2], v0[3]}), c = gelu_pk((f32x2){v1[0], v1[1]}), d = gelu_pk((f32x2){v1[2], v1[3]});
;                         v0 = (f32x4){a.x, a.y, b.x, b.y}; v1 = (f32x4){c.x, c.y, d.x, d.y}; }
;                     v0 = v0 * sc; v1 = v1 * sc; u32x4 w; w.x = cvt_pk_bf16(v0[0], v0[1]); w.y = cvt_pk_bf16(v0[2], v0[3]); w.z = cvt_pk_bf16(v1[0], v1[1]); w.w = cvt_pk_bf16(v1[2], v1[3]);
;                     *(u32x4*)(rowp + bj * HALF) = w; } }
.LBB0_190:
	v_lshl_add_u32 v156, s20, 8, v1
	v_lshl_or_b32 v148, s45, 8, v151
	s_sub_u32 s22, s6, 0x4400000
	s_subb_u32 s23, s7, 0
	s_movk_i32 s13, 0x2000
	s_movk_i32 s15, 0x600
	s_cmp_lt_u32 s45, 3
	s_cselect_b32 s13, s15, s13
	s_cselect_b32 s22, s22, s6
	s_cselect_b32 s23, s23, s7
	s_lshl_b32 s24, s13, 4
	s_lshl_b32 s25, s13, 7
	v_mul_lo_u32 v156, v156, s13
	v_lshl_add_u32 v156, v148, 1, v156
	v_add_u32_e32 v157, s24, v156
	v_add_u32_e32 v160, s25, v156
	v_add_u32_e32 v158, s24, v157
	v_add_u32_e32 v161, s24, v160
	v_add_u32_e32 v159, s24, v158
	v_add_u32_e32 v148, s24, v161
	s_nop 0
	v_add_u32_e32 v149, s24, v148
	v_cvt_pk_bf16_f32 v172, v126, v127
	v_cvt_pk_bf16_f32 v173, v128, v129
	v_cvt_pk_bf16_f32 v174, v122, v123
	v_cvt_pk_bf16_f32 v175, v124, v125
	global_store_dwordx4 v156, v[172:175], s[22:23]
	v_cvt_pk_bf16_f32 v176, v118, v119
	v_cvt_pk_bf16_f32 v177, v120, v121
	v_cvt_pk_bf16_f32 v178, v110, v111
	v_cvt_pk_bf16_f32 v179, v112, v113
	global_store_dwordx4 v156, v[176:179], s[22:23] offset:256
	v_cvt_pk_bf16_f32 v180, v114, v115
	v_cvt_pk_bf16_f32 v181, v116, v117
	v_cvt_pk_bf16_f32 v182, v106, v107
	v_cvt_pk_bf16_f32 v183, v108, v109
	global_store_dwordx4 v157, v[180:183], s[22:23]
	v_cvt_pk_bf16_f32 v184, v102, v103
	v_cvt_pk_bf16_f32 v185, v104, v105
	v_cvt_pk_bf16_f32 v186, v94, v95
	v_cvt_pk_bf16_f32 v187, v96, v97
	global_store_dwordx4 v157, v[184:187], s[22:23] offset:256
	v_cvt_pk_bf16_f32 v188, v98, v99
	v_cvt_pk_bf16_f32 v189, v100, v101
	v_cvt_pk_bf16_f32 v190, v90, v91
	v_cvt_pk_bf16_f32 v191, v92, v93
	global_store_dwordx4 v158, v[188:191], s[22:23]
	v_cvt_pk_bf16_f32 v192, v86, v87
	v_cvt_pk_bf16_f32 v193, v88, v89
	v_cvt_pk_bf16_f32 v194, v78, v79
	v_cvt_pk_bf16_f32 v195, v80, v81
	global_store_dwordx4 v158, v[192:195], s[22:23] offset:256
	v_cvt_pk_bf16_f32 v196, v82, v83
	v_cvt_pk_bf16_f32 v197, v84, v85
	v_cvt_pk_bf16_f32 v198, v74, v75
	v_cvt_pk_bf16_f32 v199, v76, v77
	global_store_dwordx4 v159, v[196:199], s[22:23]
	v_cvt_pk_bf16_f32 v200, v70, v71
	v_cvt_pk_bf16_f32 v201, v72, v73
	v_cvt_pk_bf16_f32 v202, v66, v67
	v_cvt_pk_bf16_f32 v203, v68, v69
	global_store_dwordx4 v159, v[200:203], s[22:23] offset:256
	v_cvt_pk_bf16_f32 v204, v62, v63
	v_cvt_pk_bf16_f32 v205, v64, v65
	v_cvt_pk_bf16_f32 v206, v58, v59
	v_cvt_pk_bf16_f32 v207, v60, v61
	global_store_dwordx4 v160, v[204:207], s[22:23]
	v_cvt_pk_bf16_f32 v208, v54, v55
	v_cvt_pk_bf16_f32 v209, v56, v57
	v_cvt_pk_bf16_f32 v210, v46, v47
	v_cvt_pk_bf16_f32 v211, v48, v49
	global_store_dwordx4 v160, v[208:211], s[22:23] offset:256
	v_cvt_pk_bf16_f32 v212, v50, v51
	v_cvt_pk_bf16_f32 v213, v52, v53
	v_cvt_pk_bf16_f32 v214, v42, v43
	v_cvt_pk_bf16_f32 v215, v44, v45
	global_store_dwordx4 v161, v[212:215], s[22:23]
	v_cvt_pk_bf16_f32 v216, v38, v39
	v_cvt_pk_bf16_f32 v217, v40, v41
	v_cvt_pk_bf16_f32 v218, v30, v31
	v_cvt_pk_bf16_f32 v219, v32, v33
	global_store_dwordx4 v161, v[216:219], s[22:23] offset:256
	v_cvt_pk_bf16_f32 v220, v34, v35
	v_cvt_pk_bf16_f32 v221, v36, v37
	v_cvt_pk_bf16_f32 v222, v26, v27
	v_cvt_pk_bf16_f32 v223, v28, v29
	global_store_dwordx4 v148, v[220:223], s[22:23]
	v_cvt_pk_bf16_f32 v224, v22, v23
	v_cvt_pk_bf16_f32 v225, v24, v25
	v_cvt_pk_bf16_f32 v226, v14, v15
	v_cvt_pk_bf16_f32 v227, v16, v17
	global_store_dwordx4 v148, v[224:227], s[22:23] offset:256
	v_cvt_pk_bf16_f32 v228, v18, v19
	v_cvt_pk_bf16_f32 v229, v20, v21
	v_cvt_pk_bf16_f32 v230, v10, v11
	v_cvt_pk_bf16_f32 v231, v12, v13
	global_store_dwordx4 v149, v[228:231], s[22:23]
	v_cvt_pk_bf16_f32 v236, v6, v7
	v_cvt_pk_bf16_f32 v237, v8, v9
	v_cvt_pk_bf16_f32 v238, v2, v3
	v_cvt_pk_bf16_f32 v239, v4, v5
	global_store_dwordx4 v149, v[236:239], s[22:23] offset:256
	s_andn2_b64 vcc, exec, s[2:3]
	s_mov_b64 s[2:3], -1
	s_cbranch_vccnz .LBB0_179
	s_andn2_b64 vcc, exec, s[4:5]
	s_cbranch_vccnz .LBB0_178
	s_barrier
	s_branch .LBB0_178

; #define LAS __attribute__((address_space(3)))
; DI void attn_unit(const Args& A, LAS unsigned char* lds, int unit, int tid, int wave, int lane) {
;     ...
;     const int x = unit & 15; int r0 = unit >> 4; const int hh = r0 & 3; r0 >>= 2; const int b = r0 % NB, br = r0 / NB;
;     const int dil = br == 0 ? 1 : (br == 1 ? 4 : 16), lsub = SEQ / dil, nblk = lsub / 128;
;     const int res = x / nblk, nbk = x % nblk, l0 = nbk * 128, wbase = l0 - 64;
;     LAS bf16* Qs = (LAS bf16*)(lds + AT_QS); LAS bf16* Ks = (LAS bf16*)(lds + AT_KS); LAS bf16* Vt = (LAS bf16*)(lds + AT_VT); LAS float* btab = (LAS float*)(lds + AT_BT);
;     __syncthreads();
; #pragma unroll
;     for (int i = 0; i < 2; ++i) { const int id = tid + 512 * i, row = id >> 3, ch = id & 7; const int tok = b * SEQ + (l0 + row) * dil + res;
;         *(LAS u32x4_t*)(Qs + row * AT_QLD + ch * 8) = *(const u32x4_t*)(Z + (size_t)tok * ZLD + ZA + hh * 64 + ch * 8); }
;     for (int id = tid; id < 272 * 8; id += NTHR) { const int row = id >> 3, ch = id & 7; const int pos = wbase + row; u32x4_t v = (u32x4_t){0u, 0u, 0u, 0u};
;         if (row < 256 && pos >= 0 && pos < lsub) v = *(const u32x4_t*)(Z + (size_t)(b * SEQ + pos * dil + res) * ZLD + ZA + 256 + hh * 64 + ch * 8);
;         *(LAS u32x4_t*)(Ks + row * AT_QLD + ch * 8) = v; }
;     for (int id = tid; id < 272 * 8; id += NTHR) { const int key = id % 272, ch = id / 272; const int pos = wbase + key; u32x4_t v = (u32x4_t){0u, 0u, 0u, 0u};
;         if (key < 256 && pos >= 0 && pos < lsub) v = *(const u32x4_t*)(Z + (size_t)(b * SEQ + pos * dil + res) * ZLD + ZA + 512 + hh * 64 + ch * 8);
;         LAS bf16* d = Vt + (ch * 8) * AT_VLD + key;
;         d[0] = (bf16)(v.x & 0xffffu); d[AT_VLD] = (bf16)(v.x >> 16); d[2 * AT_VLD] = (bf16)(v.y & 0xffffu); d[3 * AT_VLD] = (bf16)(v.y >> 16);
;         d[4 * AT_VLD] = (bf16)(v.z & 0xffffu); d[5 * AT_VLD] = (bf16)(v.z >> 16); d[6 * AT_VLD] = (bf16)(v.w & 0xffffu); d[7 * AT_VLD] = (bf16)(v.w >> 16); }
;     if (tid < 129) btab[tid] = A.in[I_RELB][t5_bucket((tid - 64) * dil) * 4 + hh] * 1.4426950408889634f;
.LBB0_244:
	s_cmp_lt_i32 s6, 4
	s_cselect_b64 s[0:1], -1, 0
	v_writelane_b32 v235, s0, 60
	s_nop 1
	v_writelane_b32 v235, s1, 61
	s_and_b64 s[0:1], s[0:1], s[2:3]
	s_andn2_b64 vcc, exec, s[0:1]
	v_writelane_b32 v235, s92, 62
	s_cbranch_vccnz .LBB0_496
	s_cmpk_gt_i32 s50, 0xa0
	s_cselect_b32 s0, 0x600, 0
	s_add_i32 s33, s0, s92
	s_cmpk_gt_i32 s33, 0x5ff
	s_mov_b32 s23, 0
	s_cbranch_scc1 .LBB0_336
	s_mov_b32 s6, s33
	s_mov_b32 s7, s50
	s_movk_i32 s8, 0x600
	v_readlane_b32 s9, v235, 52
	v_readlane_b32 s2, v235, 9
	v_readlane_b32 s3, v235, 10
	v_readlane_b32 s4, v235, 19
	v_readlane_b32 s5, v235, 20
	s_mov_b32 s72, 0x3e38aa3b
	s_mov_b32 s73, 0x3e38aa3b
	v_lshrrev_b32_e32 v2, 3, v0
	v_and_b32_e32 v3, 7, v0
	v_lshlrev_b32_e32 v3, 4, v3
	s_movk_i32 s39, 0x90
	v_mad_u32_u24 v1, v2, s39, v3
	v_and_b32_e32 v5, 0xff, v0
	v_lshrrev_b32_e32 v6, 8, v0
	s_movk_i32 s39, 0x1180
	v_mul_u32_u24_e32 v4, s39, v6
	v_lshl_add_u32 v4, v5, 1, v4
	v_add_u32_e32 v4, 0xe100, v4
	v_lshlrev_b32_e32 v6, 4, v6
	v_lshlrev_b32_e32 v8, 2, v5
	v_add_u32_e32 v8, 0x16d00, v8
	v_subrev_u32_e32 v165, 16, v0
	s_movk_i32 s39, 0x81
	v_cmp_gt_u32_e64 s[42:43], s39, v165
	s_movk_i32 s39, 0xa0
	v_cmp_gt_u32_e64 s[48:49], s39, v0
	v_cmp_gt_u32_e64 s[46:47], 64, v0
	v_cmp_gt_u32_e64 s[44:45], 16, v146
	v_subrev_u32_e32 v165, 0x50, v0
	v_cmp_lt_i32_e32 vcc, 0, v165
	v_mov_b32_e32 v7, 0
	s_nop 0
	v_cndmask_b32_e64 v166, 0, 16, vcc
	v_lshlrev_b32_e32 v167, 0, v165
	v_sub_u32_e32 v168, 0, v167
	v_max_i32_e32 v167, v167, v168
	v_cvt_f32_u32_e32 v168, v167
	v_mul_f32_e32 v168, 0x3e000000, v168
	v_max_f32_e32 v168, 1.0, v168
	v_log_f32_e32 v168, v168
	v_cmp_gt_u32_e32 vcc, 8, v167
	v_mul_f32_e32 v168, 0x3f924925, v168
	v_cvt_i32_f32_e32 v168, v168
	v_min_i32_e32 v168, 7, v168
	v_add_u32_e32 v168, 8, v168
	v_cndmask_b32_e32 v168, v168, v167, vcc
	v_add_u32_e32 v168, v168, v166
	v_lshl_or_b32 v7, v168, 0, v7
	v_lshlrev_b32_e32 v167, 2, v165
	v_sub_u32_e32 v168, 0, v167
	v_max_i32_e32 v167, v167, v168
	v_cvt_f32_u32_e32 v168, v167
	v_mul_f32_e32 v168, 0x3e000000, v168
	v_max_f32_e32 v168, 1.0, v168
	v_log_f32_e32 v168, v168
	v_cmp_gt_u32_e32 vcc, 8, v167
	v_mul_f32_e32 v168, 0x3f924925, v168
	v_cvt_i32_f32_e32 v168, v168
	v_min_i32_e32 v168, 7, v168
	v_add_u32_e32 v168, 8, v168
	v_cndmask_b32_e32 v168, v168, v167, vcc
	v_add_u32_e32 v168, v168, v166
	v_lshl_or_b32 v7, v168, 8, v7
	v_lshlrev_b32_e32 v167, 4, v165
	v_sub_u32_e32 v168, 0, v167
	v_max_i32_e32 v167, v167, v168
	v_cvt_f32_u32_e32 v168, v167
	v_mul_f32_e32 v168, 0x3e000000, v168
	v_max_f32_e32 v168, 1.0, v168
	v_log_f32_e32 v168, v168
	v_cmp_gt_u32_e32 vcc, 8, v167
	v_mul_f32_e32 v168, 0x3f924925, v168
	v_cvt_i32_f32_e32 v168, v168
	v_min_i32_e32 v168, 7, v168
	v_add_u32_e32 v168, 8, v168
	v_cndmask_b32_e32 v168, v168, v167, vcc
	v_add_u32_e32 v168, v168, v166
	v_lshl_or_b32 v7, v168, 16, v7
	v_and_b32_e32 v165, 15, v146
	v_lshrrev_b32_e32 v166, 4, v146
	s_lshl_b32 s39, s9, 4
	v_add_u32_e32 v40, s39, v165
	s_movk_i32 s40, 0x90
	v_mul_u32_u24_e32 v34, s40, v40
	v_lshl_add_u32 v34, v166, 4, v34
	v_lshlrev_b32_e32 v167, 2, v166
	v_sub_u32_e32 v35, v167, v165
	v_lshlrev_b32_e32 v35, 2, v35
	v_add_u32_e32 v35, 0x16d40, v35
	v_add_u32_e32 v167, s39, v167
	v_lshlrev_b32_e32 v36, 2, v167
	v_add_u32_e32 v36, 0x16f80, v36
	s_movk_i32 s40, 0x230
	v_mul_u32_u24_e32 v37, s40, v165
	v_lshl_add_u32 v37, v167, 1, v37
	v_add_u32_e32 v37, 0xe100, v37
	v_add_u32_e32 v9, 0x2300, v37
	v_add_u32_e32 v118, 0x4600, v37
	v_add_u32_e32 v144, 0x6900, v37
	v_xor_b32_e32 v38, 16, v146
	v_lshlrev_b32_e32 v38, 2, v38
	v_xor_b32_e32 v39, 32, v146
	v_lshlrev_b32_e32 v39, 2, v39
	v_lshlrev_b32_e32 v41, 3, v166
	v_mov_b32_e32 v232, 0
	v_mov_b32_e32 v233, 0
	s_movk_i32 s40, 0x230
	v_mul_u32_u24_e32 v168, s40, v0
	v_add_u32_e32 v168, 0xe300, v168
	s_and_saveexec_b64 s[40:41], s[46:47]
	ds_write_b64 v168, v[232:233] offset:0
	ds_write_b64 v168, v[232:233] offset:8
	ds_write_b64 v168, v[232:233] offset:16
	ds_write_b64 v168, v[232:233] offset:24
	s_mov_b64 exec, s[40:41]
	s_and_b32 s39, s6, 15
	s_bfe_u32 s40, s6, 0x20004
	s_bfe_u32 s41, s6, 0x30006
	s_lshr_b32 s74, s6, 9
	s_lshl_b32 s75, s74, 1
	s_lshl_b32 s16, 1536, s75
	s_add_i32 s20, s75, 9
	s_add_i32 s26, s75, 4
	s_lshl_b32 s28, s74, 3
	s_lshr_b32 s29, 0x800, s75
	s_add_i32 s17, s29, -1
	s_sub_i32 s76, 4, s75
	s_lshr_b32 s77, s39, s76
	s_lshr_b32 s78, 16, s75
	s_add_i32 s78, s78, -1
	s_and_b32 s78, s39, s78
	s_lshl_b32 s19, s78, 7
	s_add_i32 s18, s19, 0xffffffc0
	s_lshl_b32 s79, s41, 11
	s_add_i32 s79, s79, s77
	s_lshl_b32 s80, s40, 7
	s_lshl_b32 s27, s40, 2
	s_mul_i32 s81, s79, 1536
	s_add_u32 s81, s81, s80
	s_add_u32 s81, s81, 0x28600000
	s_add_u32 s10, s2, s81
	s_addc_u32 s11, s3, 0
	s_lshl_b32 s82, s74, 14
	s_add_i32 s82, s82, s79
	s_lshl_b32 s83, s82, 9
	s_add_u32 s83, s83, s80
	s_add_u32 s83, s83, 0x34a00000
	s_add_u32 s12, s2, s83
	s_addc_u32 s13, s3, 0
	s_lshl_b32 s84, s82, 4
	s_add_u32 s84, s84, s27
	s_add_u32 s84, s84, 0x36200000
	s_add_u32 s14, s2, s84
	s_addc_u32 s15, s3, 0
	v_add_u32_e32 v165, s19, v2
	v_mad_u32_u24 v165, v165, s16, v3
	s_lshl_b32 s85, s16, 6
	global_load_dwordx4 v[120:123], v165, s[10:11]
	v_add_u32_e32 v166, s85, v165
	global_load_dwordx4 v[124:127], v166, s[10:11]
	v_add_u32_e32 v167, s18, v2
	v_med3_i32 v168, v167, 0, s17
	v_mad_u32_u24 v168, v168, s16, v3
	global_load_dwordx4 v[128:131], v168, s[10:11] offset:512
	v_add_u32_e32 v168, 64, v167
	v_med3_i32 v168, v168, 0, s17
	v_mad_u32_u24 v168, v168, s16, v3
	global_load_dwordx4 v[132:135], v168, s[10:11] offset:512
	v_add_u32_e32 v168, 0x80, v167
	v_med3_i32 v168, v168, 0, s17
	v_mad_u32_u24 v168, v168, s16, v3
	global_load_dwordx4 v[136:139], v168, s[10:11] offset:512
	v_add_u32_e32 v168, 0xc0, v167
	v_med3_i32 v168, v168, 0, s17
	v_mad_u32_u24 v168, v168, s16, v3
	global_load_dwordx4 v[140:143], v168, s[10:11] offset:512
	v_add_u32_e32 v169, s18, v5
	v_med3_i32 v169, v169, 0, s17
	v_mad_u32_u24 v169, v169, s16, v6
	global_load_dwordx4 v[148:151], v169, s[10:11] offset:1024
	global_load_dwordx4 v[152:155], v169, s[10:11] offset:1056
	global_load_dwordx4 v[156:159], v169, s[10:11] offset:1088
	global_load_dwordx4 v[160:163], v169, s[10:11] offset:1120
	v_bfe_u32 v171, v7, s28, 8
	v_lshl_add_u32 v171, v171, 4, s27
	s_mov_b64 exec, s[42:43]
	global_load_dword v164, v171, s[4:5]
	s_mov_b64 exec, -1
; #define LAS __attribute__((address_space(3)))
; DI void attn_unit(const Args& A, LAS unsigned char* lds, int unit, int tid, int wave, int lane) {
;     ...
;     __syncthreads();
; #pragma unroll
;     for (int i = 0; i < 2; ++i) { const int id = tid + 512 * i, row = id >> 3, ch = id & 7; const int tok = b * SEQ + (l0 + row) * dil + res;
;         *(LAS u32x4_t*)(Qs + row * AT_QLD + ch * 8) = *(const u32x4_t*)(Z + (size_t)tok * ZLD + ZA + hh * 64 + ch * 8); }
;     for (int id = tid; id < 272 * 8; id += NTHR) { const int row = id >> 3, ch = id & 7; const int pos = wbase + row; u32x4_t v = (u32x4_t){0u, 0u, 0u, 0u};
;         if (row < 256 && pos >= 0 && pos < lsub) v = *(const u32x4_t*)(Z + (size_t)(b * SEQ + pos * dil + res) * ZLD + ZA + 256 + hh * 64 + ch * 8);
;         *(LAS u32x4_t*)(Ks + row * AT_QLD + ch * 8) = v; }
;     for (int id = tid; id < 272 * 8; id += NTHR) { const int key = id % 272, ch = id / 272; const int pos = wbase + key; u32x4_t v = (u32x4_t){0u, 0u, 0u, 0u};
;         if (key < 256 && pos >= 0 && pos < lsub) v = *(const u32x4_t*)(Z + (size_t)(b * SEQ + pos * dil + res) * ZLD + ZA + 512 + hh * 64 + ch * 8);
;         LAS bf16* d = Vt + (ch * 8) * AT_VLD + key;
;         d[0] = (bf16)(v.x & 0xffffu); d[AT_VLD] = (bf16)(v.x >> 16); d[2 * AT_VLD] = (bf16)(v.y & 0xffffu); d[3 * AT_VLD] = (bf16)(v.y >> 16);
;         d[4 * AT_VLD] = (bf16)(v.z & 0xffffu); d[5 * AT_VLD] = (bf16)(v.z >> 16); d[6 * AT_VLD] = (bf16)(v.w & 0xffffu); d[7 * AT_VLD] = (bf16)(v.w >> 16); }
;     if (tid < 129) btab[tid] = A.in[I_RELB][t5_bucket((tid - 64) * dil) * 4 + hh] * 1.4426950408889634f;
;     __syncthreads();
.LatA_loop:
	s_barrier
	s_mov_b64 s[30:31], s[12:13]
	s_mov_b64 s[32:33], s[14:15]
	s_mov_b32 s34, s19
	s_mov_b32 s35, s20
	s_mov_b32 s36, s26
	s_mov_b32 s37, s18
	s_mov_b32 s38, s29
	v_add_u32_e32 v165, s37, v5
	v_cmp_gt_u32_e32 vcc, s38, v165
	v_mov_b32_e32 v166, 0xf149f2ca
	s_nop 0
	v_cndmask_b32_e64 v165, v166, 0, vcc
	ds_write_b32 v8, v165 offset:640
	s_waitcnt vmcnt(0)
	ds_write_b128 v1, v[120:123]
	ds_write_b128 v1, v[124:127] offset:9216
	ds_write_b128 v1, v[128:131] offset:18432
	ds_write_b128 v1, v[132:135] offset:27648
	ds_write_b128 v1, v[136:139] offset:36864
	ds_write_b128 v1, v[140:143] offset:46080
	ds_write_b16 v4, v148 offset:0
	ds_write_b16_d16_hi v4, v148 offset:560
	ds_write_b16 v4, v149 offset:1120
	ds_write_b16_d16_hi v4, v149 offset:1680
	ds_write_b16 v4, v150 offset:2240
	ds_write_b16_d16_hi v4, v150 offset:2800
	ds_write_b16 v4, v151 offset:3360
	ds_write_b16_d16_hi v4, v151 offset:3920
	ds_write_b16 v4, v152 offset:8960
	ds_write_b16_d16_hi v4, v152 offset:9520
	ds_write_b16 v4, v153 offset:10080
	ds_write_b16_d16_hi v4, v153 offset:10640
	ds_write_b16 v4, v154 offset:11200
	ds_write_b16_d16_hi v4, v154 offset:11760
	ds_write_b16 v4, v155 offset:12320
	ds_write_b16_d16_hi v4, v155 offset:12880
	ds_write_b16 v4, v156 offset:17920
	ds_write_b16_d16_hi v4, v156 offset:18480
	ds_write_b16 v4, v157 offset:19040
	ds_write_b16_d16_hi v4, v157 offset:19600
	ds_write_b16 v4, v158 offset:20160
	ds_write_b16_d16_hi v4, v158 offset:20720
	ds_write_b16 v4, v159 offset:21280
	ds_write_b16_d16_hi v4, v159 offset:21840
	ds_write_b16 v4, v160 offset:26880
	ds_write_b16_d16_hi v4, v160 offset:27440
	ds_write_b16 v4, v161 offset:28000
	ds_write_b16_d16_hi v4, v161 offset:28560
	ds_write_b16 v4, v162 offset:29120
	ds_write_b16_d16_hi v4, v162 offset:29680
	ds_write_b16 v4, v163 offset:30240
	ds_write_b16_d16_hi v4, v163 offset:30800
	v_mul_f32_e32 v167, 0x3fb8aa3b, v164
	v_cndmask_b32_e64 v167, v166, v167, s[42:43]
	s_mov_b64 exec, s[48:49]
	ds_write_b32 v8, v167
	s_mov_b64 exec, -1
	s_add_i32 s6, s6, s7
	s_cmp_lt_i32 s6, s8
	s_cbranch_scc0 .LatA_nopf
	s_and_b32 s39, s6, 15
	s_bfe_u32 s40, s6, 0x20004
	s_bfe_u32 s41, s6, 0x30006
	s_lshr_b32 s74, s6, 9
	s_lshl_b32 s75, s74, 1
	s_lshl_b32 s16, 1536, s75
	s_add_i32 s20, s75, 9
	s_add_i32 s26, s75, 4
	s_lshl_b32 s28, s74, 3
	s_lshr_b32 s29, 0x800, s75
	s_add_i32 s17, s29, -1
	s_sub_i32 s76, 4, s75
	s_lshr_b32 s77, s39, s76
	s_lshr_b32 s78, 16, s75
	s_add_i32 s78, s78, -1
	s_and_b32 s78, s39, s78
	s_lshl_b32 s19, s78, 7
	s_add_i32 s18, s19, 0xffffffc0
	s_lshl_b32 s79, s41, 11
	s_add_i32 s79, s79, s77
	s_lshl_b32 s80, s40, 7
	s_lshl_b32 s27, s40, 2
	s_mul_i32 s81, s79, 1536
	s_add_u32 s81, s81, s80
	s_add_u32 s81, s81, 0x28600000
	s_add_u32 s10, s2, s81
	s_addc_u32 s11, s3, 0
	s_lshl_b32 s82, s74, 14
	s_add_i32 s82, s82, s79
	s_lshl_b32 s83, s82, 9
	s_add_u32 s83, s83, s80
	s_add_u32 s83, s83, 0x34a00000
	s_add_u32 s12, s2, s83
	s_addc_u32 s13, s3, 0
	s_lshl_b32 s84, s82, 4
	s_add_u32 s84, s84, s27
	s_add_u32 s84, s84, 0x36200000
	s_add_u32 s14, s2, s84
	s_addc_u32 s15, s3, 0
	v_add_u32_e32 v165, s19, v2
	v_mad_u32_u24 v165, v165, s16, v3
	s_lshl_b32 s85, s16, 6
	global_load_dwordx4 v[120:123], v165, s[10:11]
	v_add_u32_e32 v166, s85, v165
	global_load_dwordx4 v[124:127], v166, s[10:11]
	v_add_u32_e32 v167, s18, v2
	v_med3_i32 v168, v167, 0, s17
	v_mad_u32_u24 v168, v168, s16, v3
	global_load_dwordx4 v[128:131], v168, s[10:11] offset:512
	v_add_u32_e32 v168, 64, v167
	v_med3_i32 v168, v168, 0, s17
	v_mad_u32_u24 v168, v168, s16, v3
	global_load_dwordx4 v[132:135], v168, s[10:11] offset:512
	v_add_u32_e32 v168, 0x80, v167
	v_med3_i32 v168, v168, 0, s17
	v_mad_u32_u24 v168, v168, s16, v3
	global_load_dwordx4 v[136:139], v168, s[10:11] offset:512
	v_add_u32_e32 v168, 0xc0, v167
	v_med3_i32 v168, v168, 0, s17
	v_mad_u32_u24 v168, v168, s16, v3
	global_load_dwordx4 v[140:143], v168, s[10:11] offset:512
	v_add_u32_e32 v169, s18, v5
	v_med3_i32 v169, v169, 0, s17
	v_mad_u32_u24 v169, v169, s16, v6
	global_load_dwordx4 v[148:151], v169, s[10:11] offset:1024
	global_load_dwordx4 v[152:155], v169, s[10:11] offset:1056
	global_load_dwordx4 v[156:159], v169, s[10:11] offset:1088
	global_load_dwordx4 v[160:163], v169, s[10:11] offset:1120
	v_bfe_u32 v171, v7, s28, 8
	v_lshl_add_u32 v171, v171, 4, s27
	s_mov_b64 exec, s[42:43]
	global_load_dword v164, v171, s[4:5]
	s_mov_b64 exec, -1

; DI void attn_unit(const Args& A, LAS unsigned char* lds, int unit, int tid, int wave, int lane) {
;     ...
;     const int x = unit & 15; int r0 = unit >> 4; const int hh = r0 & 3; r0 >>= 2; const int b = r0 % NB, br = r0 / NB;
;     const int dil = br == 0 ? 1 : (br == 1 ? 4 : 16), lsub = SEQ / dil, nblk = lsub / 128;
;     const int res = x / nblk, nbk = x % nblk, l0 = nbk * 128, wbase = l0 - 64;
;     LAS bf16* Qs = (LAS bf16*)(lds + AT_QS); LAS bf16* Ks = (LAS bf16*)(lds + AT_KS); LAS bf16* Vt = (LAS bf16*)(lds + AT_VT); LAS float* btab = (LAS float*)(lds + AT_BT);
;     __syncthreads();
; #pragma unroll
;     for (int i = 0; i < 2; ++i) { const int id = tid + 512 * i, row = id >> 3, ch = id & 7; const int tok = b * SEQ + (l0 + row) * dil + res;
;         *(LAS u32x4_t*)(Qs + row * AT_QLD + ch * 8) = *(const u32x4_t*)(Z + (size_t)tok * ZLD + ZA + hh * 64 + ch * 8); }
;     for (int id = tid; id < 272 * 8; id += NTHR) { const int row = id >> 3, ch = id & 7; const int pos = wbase + row; u32x4_t v = (u32x4_t){0u, 0u, 0u, 0u};
;         if (row < 256 && pos >= 0 && pos < lsub) v = *(const u32x4_t*)(Z + (size_t)(b * SEQ + pos * dil + res) * ZLD + ZA + 256 + hh * 64 + ch * 8);
;         *(LAS u32x4_t*)(Ks + row * AT_QLD + ch * 8) = v; }
;     for (int id = tid; id < 272 * 8; id += NTHR) { const int key = id % 272, ch = id / 272; const int pos = wbase + key; u32x4_t v = (u32x4_t){0u, 0u, 0u, 0u};
;         if (key < 256 && pos >= 0 && pos < lsub) v = *(const u32x4_t*)(Z + (size_t)(b * SEQ + pos * dil + res) * ZLD + ZA + 512 + hh * 64 + ch * 8);
;         LAS bf16* d = Vt + (ch * 8) * AT_VLD + key;
;         d[0] = (bf16)(v.x & 0xffffu); d[AT_VLD] = (bf16)(v.x >> 16); d[2 * AT_VLD] = (bf16)(v.y & 0xffffu); d[3 * AT_VLD] = (bf16)(v.y >> 16);
;         d[4 * AT_VLD] = (bf16)(v.z & 0xffffu); d[5 * AT_VLD] = (bf16)(v.z >> 16); d[6 * AT_VLD] = (bf16)(v.w & 0xffffu); d[7 * AT_VLD] = (bf16)(v.w >> 16); }
;     if (tid < 129) btab[tid] = A.in[I_RELB][t5_bucket((tid - 64) * dil) * 4 + hh] * 1.4426950408889634f;
; template <int l> DI void run_layer(const Args& A, LAS unsigned char* lds, const XcdBarrier& bar, int lo, int hi, int G, int bid, int tid, int lane, int wave, int gw, int ngw, int gtid, int nthr) {
;     ...
;     PH(3,
;           if (G > ATT_SCAN_BLK0 && bid >= ATT_SCAN_BLK0) phase_attn(A, lds, 0, ATT_UNITS - ATT_SPLIT, bid - ATT_SCAN_BLK0, G - ATT_SCAN_BLK0, tid, wave, lane);
.LBB0_546:
	s_cmp_lt_i32 s6, 5
	s_cselect_b64 s[94:95], -1, 0
	s_and_b64 s[0:1], s[94:95], s[0:1]
	s_andn2_b64 vcc, exec, s[0:1]
	s_cbranch_vccnz .LBB0_957
	s_cmpk_lt_i32 s50, 0xa1
	s_cselect_b64 s[0:1], -1, 0
	s_cmpk_lt_i32 s92, 0xa0
	s_cselect_b64 s[2:3], -1, 0
	s_or_b64 s[0:1], s[2:3], s[0:1]
	s_and_b64 vcc, exec, s[0:1]
	s_cbranch_vccnz .LBB0_640
	s_add_i32 s22, s92, 0xffffff60
	s_cmpk_gt_u32 s22, 0x23f
	s_cbranch_scc1 .LBB0_639
	s_mov_b32 s6, s22
	s_add_i32 s7, s50, 0xffffff60
	s_movk_i32 s8, 0x600
	v_readlane_b32 s9, v235, 52
	v_readlane_b32 s2, v235, 9
	v_readlane_b32 s3, v235, 10
	v_readlane_b32 s4, v235, 19
	v_readlane_b32 s5, v235, 20
	s_mov_b32 s72, 0x3e38aa3b
	s_mov_b32 s73, 0x3e38aa3b
	v_lshrrev_b32_e32 v2, 3, v0
	v_and_b32_e32 v3, 7, v0
	v_lshlrev_b32_e32 v3, 4, v3
	s_movk_i32 s39, 0x90
	v_mad_u32_u24 v1, v2, s39, v3
	v_and_b32_e32 v5, 0xff, v0
	v_lshrrev_b32_e32 v6, 8, v0
	s_movk_i32 s39, 0x1180
	v_mul_u32_u24_e32 v4, s39, v6
	v_lshl_add_u32 v4, v5, 1, v4
	v_add_u32_e32 v4, 0xe100, v4
	v_lshlrev_b32_e32 v6, 4, v6
	v_lshlrev_b32_e32 v8, 2, v5
	v_add_u32_e32 v8, 0x16d00, v8
	v_subrev_u32_e32 v165, 16, v0
	s_movk_i32 s39, 0x81
	v_cmp_gt_u32_e64 s[42:43], s39, v165
	s_movk_i32 s39, 0xa0
	v_cmp_gt_u32_e64 s[48:49], s39, v0
	v_cmp_gt_u32_e64 s[46:47], 64, v0
	v_cmp_gt_u32_e64 s[44:45], 16, v146
	v_subrev_u32_e32 v165, 0x50, v0
	v_cmp_lt_i32_e32 vcc, 0, v165
	v_mov_b32_e32 v7, 0
	s_nop 0
	v_cndmask_b32_e64 v166, 0, 16, vcc
	v_lshlrev_b32_e32 v167, 0, v165
	v_sub_u32_e32 v168, 0, v167
	v_max_i32_e32 v167, v167, v168
	v_cvt_f32_u32_e32 v168, v167
	v_mul_f32_e32 v168, 0x3e000000, v168
	v_max_f32_e32 v168, 1.0, v168
	v_log_f32_e32 v168, v168
	v_cmp_gt_u32_e32 vcc, 8, v167
	v_mul_f32_e32 v168, 0x3f924925, v168
	v_cvt_i32_f32_e32 v168, v168
	v_min_i32_e32 v168, 7, v168
	v_add_u32_e32 v168, 8, v168
	v_cndmask_b32_e32 v168, v168, v167, vcc
	v_add_u32_e32 v168, v168, v166
	v_lshl_or_b32 v7, v168, 0, v7
	v_lshlrev_b32_e32 v167, 2, v165
	v_sub_u32_e32 v168, 0, v167
	v_max_i32_e32 v167, v167, v168
	v_cvt_f32_u32_e32 v168, v167
	v_mul_f32_e32 v168, 0x3e000000, v168
	v_max_f32_e32 v168, 1.0, v168
	v_log_f32_e32 v168, v168
	v_cmp_gt_u32_e32 vcc, 8, v167
	v_mul_f32_e32 v168, 0x3f924925, v168
	v_cvt_i32_f32_e32 v168, v168
	v_min_i32_e32 v168, 7, v168
	v_add_u32_e32 v168, 8, v168
	v_cndmask_b32_e32 v168, v168, v167, vcc
	v_add_u32_e32 v168, v168, v166
	v_lshl_or_b32 v7, v168, 8, v7
	v_lshlrev_b32_e32 v167, 4, v165
	v_sub_u32_e32 v168, 0, v167
	v_max_i32_e32 v167, v167, v168
	v_cvt_f32_u32_e32 v168, v167
	v_mul_f32_e32 v168, 0x3e000000, v168
	v_max_f32_e32 v168, 1.0, v168
	v_log_f32_e32 v168, v168
	v_cmp_gt_u32_e32 vcc, 8, v167
	v_mul_f32_e32 v168, 0x3f924925, v168
	v_cvt_i32_f32_e32 v168, v168
	v_min_i32_e32 v168, 7, v168
	v_add_u32_e32 v168, 8, v168
	v_cndmask_b32_e32 v168, v168, v167, vcc
	v_add_u32_e32 v168, v168, v166
	v_lshl_or_b32 v7, v168, 16, v7
	v_and_b32_e32 v165, 15, v146
	v_lshrrev_b32_e32 v166, 4, v146
	s_lshl_b32 s39, s9, 4
	v_add_u32_e32 v40, s39, v165
	s_movk_i32 s40, 0x90
	v_mul_u32_u24_e32 v34, s40, v40
	v_lshl_add_u32 v34, v166, 4, v34
	v_lshlrev_b32_e32 v167, 2, v166
	v_sub_u32_e32 v35, v167, v165
	v_lshlrev_b32_e32 v35, 2, v35
	v_add_u32_e32 v35, 0x16d40, v35
	v_add_u32_e32 v167, s39, v167
	v_lshlrev_b32_e32 v36, 2, v167
	v_add_u32_e32 v36, 0x16f80, v36
	s_movk_i32 s40, 0x230
	v_mul_u32_u24_e32 v37, s40, v165
	v_lshl_add_u32 v37, v167, 1, v37
	v_add_u32_e32 v37, 0xe100, v37
	v_add_u32_e32 v9, 0x2300, v37
	v_add_u32_e32 v118, 0x4600, v37
	v_add_u32_e32 v144, 0x6900, v37
	v_xor_b32_e32 v38, 16, v146
	v_lshlrev_b32_e32 v38, 2, v38
	v_xor_b32_e32 v39, 32, v146
	v_lshlrev_b32_e32 v39, 2, v39
	v_lshlrev_b32_e32 v41, 3, v166
	v_mov_b32_e32 v232, 0
	v_mov_b32_e32 v233, 0
	s_movk_i32 s40, 0x230
	v_mul_u32_u24_e32 v168, s40, v0
	v_add_u32_e32 v168, 0xe300, v168
	s_and_saveexec_b64 s[40:41], s[46:47]
	ds_write_b64 v168, v[232:233] offset:0
	ds_write_b64 v168, v[232:233] offset:8
	ds_write_b64 v168, v[232:233] offset:16
	ds_write_b64 v168, v[232:233] offset:24
	s_mov_b64 exec, s[40:41]
	s_and_b32 s39, s6, 15
	s_bfe_u32 s40, s6, 0x20004
	s_bfe_u32 s41, s6, 0x30006
	s_lshr_b32 s74, s6, 9
	s_lshl_b32 s75, s74, 1
	s_lshl_b32 s16, 1536, s75
	s_add_i32 s20, s75, 9
	s_add_i32 s26, s75, 4
	s_lshl_b32 s28, s74, 3
	s_lshr_b32 s29, 0x800, s75
	s_add_i32 s17, s29, -1
	s_sub_i32 s76, 4, s75
	s_lshr_b32 s77, s39, s76
	s_lshr_b32 s78, 16, s75
	s_add_i32 s78, s78, -1
	s_and_b32 s78, s39, s78
	s_lshl_b32 s19, s78, 7
	s_add_i32 s18, s19, 0xffffffc0
	s_lshl_b32 s79, s41, 11
	s_add_i32 s79, s79, s77
	s_lshl_b32 s80, s40, 7
	s_lshl_b32 s27, s40, 2
	s_mul_i32 s81, s79, 1536
	s_add_u32 s81, s81, s80
	s_add_u32 s81, s81, 0x28600000
	s_add_u32 s10, s2, s81
	s_addc_u32 s11, s3, 0
	s_lshl_b32 s82, s74, 14
	s_add_i32 s82, s82, s79
	s_lshl_b32 s83, s82, 9
	s_add_u32 s83, s83, s80
	s_add_u32 s83, s83, 0x34a00000
	s_add_u32 s12, s2, s83
	s_addc_u32 s13, s3, 0
	s_lshl_b32 s84, s82, 4
	s_add_u32 s84, s84, s27
	s_add_u32 s84, s84, 0x36200000
	s_add_u32 s14, s2, s84
	s_addc_u32 s15, s3, 0
	v_add_u32_e32 v165, s19, v2
	v_mad_u32_u24 v165, v165, s16, v3
	s_lshl_b32 s85, s16, 6
	global_load_dwordx4 v[120:123], v165, s[10:11]
	v_add_u32_e32 v166, s85, v165
	global_load_dwordx4 v[124:127], v166, s[10:11]
	v_add_u32_e32 v167, s18, v2
	v_med3_i32 v168, v167, 0, s17
	v_mad_u32_u24 v168, v168, s16, v3
	global_load_dwordx4 v[128:131], v168, s[10:11] offset:512
	v_add_u32_e32 v168, 64, v167
	v_med3_i32 v168, v168, 0, s17
	v_mad_u32_u24 v168, v168, s16, v3
	global_load_dwordx4 v[132:135], v168, s[10:11] offset:512
	v_add_u32_e32 v168, 0x80, v167
	v_med3_i32 v168, v168, 0, s17
	v_mad_u32_u24 v168, v168, s16, v3
	global_load_dwordx4 v[136:139], v168, s[10:11] offset:512
	v_add_u32_e32 v168, 0xc0, v167
	v_med3_i32 v168, v168, 0, s17
	v_mad_u32_u24 v168, v168, s16, v3
	global_load_dwordx4 v[140:143], v168, s[10:11] offset:512
	v_add_u32_e32 v169, s18, v5
	v_med3_i32 v169, v169, 0, s17
	v_mad_u32_u24 v169, v169, s16, v6
	global_load_dwordx4 v[148:151], v169, s[10:11] offset:1024
	global_load_dwordx4 v[152:155], v169, s[10:11] offset:1056
	global_load_dwordx4 v[156:159], v169, s[10:11] offset:1088
	global_load_dwordx4 v[160:163], v169, s[10:11] offset:1120
	v_bfe_u32 v171, v7, s28, 8
	v_lshl_add_u32 v171, v171, 4, s27
	s_mov_b64 exec, s[42:43]
	global_load_dword v164, v171, s[4:5]
	s_mov_b64 exec, -1

; __device__ __forceinline__ unsigned xb_add(unsigned* p, unsigned v) { return __hip_atomic_fetch_add(p, v, __ATOMIC_RELAXED, __HIP_MEMORY_SCOPE_AGENT); }
; __device__ __forceinline__ void xcd_barrier(const XcdBarrier& b) {
;     asm volatile("s_waitcnt vmcnt(0)" ::: "memory");
;     __syncthreads();
;     if (threadIdx.x == 0) {
;         unsigned* bar = b.bar;
;         __builtin_amdgcn_s_waitcnt(0);
;         unsigned nloc = b.st[0], nx = b.st[1];
;         if (nloc == 0u) { xcd_barrier_complete(bar, b.x, nloc, nx); b.st[0] = nloc; b.st[1] = nx; }
;         const unsigned old = xb_add(&bar[XB_XSUB(b.x)], 1u);
; template <int l> DI void run_layer(const Args& A, LAS unsigned char* lds, const XcdBarrier& bar, int lo, int hi, int G, int bid, int tid, int lane, int wave, int gw, int ngw, int gtid, int nthr) {
;     ...
;           for (int rep = 0; rep < 1 + ((MK_DUP >> 14) & 1); ++rep) for (int u = bid; u < 96; u += G) rwkv_r2_unit(A, lds, u, tid, wave, lane);
;           for (int rep = 0; rep < 1 + ((MK_DUP >> 15) & 1); ++rep) for (int u = bid; u < 96 + 64; u += G) { if (u >= 96) mlstm_m2_unit(A, lds, u - 96, tid, wave, lane); });
.Lm20_unext:
	s_add_i32 s6, s6, s50
	s_branch .Lm20_uloop
.LBB0_957:
	v_readlane_b32 s4, v235, 9
	v_readlane_b32 s7, v235, 12
	s_cmp_gt_i32 s7, 5
	s_cselect_b64 s[0:1], -1, 0
	s_and_b64 s[2:3], s[94:95], s[0:1]
	v_readlane_b32 s5, v235, 10
	v_readlane_b32 s6, v235, 11
	s_andn2_b64 vcc, exec, s[2:3]
	s_cbranch_vccnz .LBB0_1007
	s_waitcnt vmcnt(0)
	v_cmp_eq_u32_e32 vcc, 0, v0
	s_waitcnt vmcnt(0)
	s_barrier
	s_and_saveexec_b64 s[2:3], vcc
	s_cbranch_execz .LBB0_1006
	s_add_i32 s4, 0, 0x23f20
	v_mov_b32_e32 v1, s4
	s_waitcnt vmcnt(0) expcnt(0) lgkmcnt(0)
	ds_read_b32 v3, v1
	s_add_i32 s4, 0, 0x23f24
	v_mov_b32_e32 v1, s4
	ds_read_b32 v1, v1
	s_waitcnt lgkmcnt(1)
	v_cmp_ne_u32_e32 vcc, 0, v3
	s_cbranch_vccnz .LBB0_974
	v_readlane_b32 s4, v235, 13
	v_readlane_b32 s5, v235, 14
	s_load_dwordx2 s[8:9], s[4:5], 0x4
	v_readlane_b32 s40, v235, 9
	v_readlane_b32 s41, v235, 10
	s_add_u32 s4, s40, 0x4200
	s_addc_u32 s5, s41, 0
	s_add_u32 s6, s40, 0x4400
	s_addc_u32 s7, s41, 0
	s_waitcnt lgkmcnt(0)
	s_mul_i32 s33, s8, s50
	s_add_u32 s8, s40, 0x4500
	s_mul_i32 s33, s33, s9
	s_addc_u32 s9, s41, 0
	s_add_u32 s10, s40, 0x4600
	s_addc_u32 s11, s41, 0
	s_add_u32 s12, s40, 0x4700
	s_addc_u32 s13, s41, 0
	s_add_u32 s14, s40, 0x4800
	s_addc_u32 s15, s41, 0
	s_add_u32 s16, s40, 0x4900
	s_addc_u32 s17, s41, 0
	s_add_u32 s18, s40, 0x4a00
	s_addc_u32 s19, s41, 0
	s_add_u32 s20, s40, 0x4b00
	s_addc_u32 s21, s41, 0
	s_add_u32 s22, s40, 0x4c00
	s_addc_u32 s23, s41, 0
	s_add_u32 s24, s40, 0x4d00
	s_addc_u32 s25, s41, 0
	s_add_u32 s26, s40, 0x4e00
	s_addc_u32 s27, s41, 0
	s_add_u32 s28, s40, 0x4f00
	s_addc_u32 s29, s41, 0
	s_add_u32 s30, s40, 0x5000
	s_addc_u32 s31, s41, 0
	s_add_u32 s34, s40, 0x5100
	s_addc_u32 s35, s41, 0
	s_add_u32 s36, s40, 0x5200
	s_addc_u32 s37, s41, 0
	s_add_u32 s38, s40, 0x5300
	s_addc_u32 s39, s41, 0
	s_mov_b32 s46, 1
	v_mov_b32_e32 v17, 0
	v_readlane_b32 s42, v235, 11
	v_readlane_b32 s43, v235, 12
	s_branch .LBB0_962

; __device__ __forceinline__ unsigned cvt_pk_bf16(float lo, float hi) { unsigned r; asm volatile("v_cvt_pk_bf16_f32 %0, %1, %2" : "=v"(r) : "v"(lo), "v"(hi)); return r; }
;     __device__ __forceinline__ void operator()(const f32x4 (&acc)[2][2][4][2], const Unit& u, int wr, int wc, int fr, int fq) const {
;     ...
;             for (int m = 0; m < 4; ++m) { bf16_t* rowp = base + (size_t)(row0 + ai * HALF + m * 16) * ldc + col0;
; #pragma unroll
;                 for (int bj = 0; bj < 2; ++bj) { f32x4 v0 = acc[ai][bj][m][0] + bv[bj][0], v1 = acc[ai][bj][m][1] + bv[bj][1];
;                     if (ACT == 1) { f32x2 a = gelu_pk((f32x2){v0[0], v0[1]}), b = gelu_pk((f32x2){v0[2], v0[3]}), c = gelu_pk((f32x2){v1[0], v1[1]}), d = gelu_pk((f32x2){v1[2], v1[3]});
;                         v0 = (f32x4){a.x, a.y, b.x, b.y}; v1 = (f32x4){c.x, c.y, d.x, d.y}; }
;                     v0 = v0 * sc; v1 = v1 * sc; u32x4 w; w.x = cvt_pk_bf16(v0[0], v0[1]); w.y = cvt_pk_bf16(v0[2], v0[3]); w.z = cvt_pk_bf16(v1[0], v1[1]); w.w = cvt_pk_bf16(v1[2], v1[3]);
;                     *(u32x4*)(rowp + bj * HALF) = w; } }
.LBB0_1650:
	v_lshl_add_u32 v156, s20, 8, v1
	v_lshl_or_b32 v148, s44, 8, v151
	s_sub_u32 s22, s6, 0x4400000
	s_subb_u32 s23, s7, 0
	s_movk_i32 s13, 0x2000
	s_movk_i32 s15, 0x600
	s_cmp_lt_u32 s44, 3
	s_cselect_b32 s13, s15, s13
	s_cselect_b32 s22, s22, s6
	s_cselect_b32 s23, s23, s7
	s_lshl_b32 s24, s13, 4
	s_lshl_b32 s25, s13, 7
	v_mul_lo_u32 v156, v156, s13
	v_lshl_add_u32 v156, v148, 1, v156
	v_add_u32_e32 v157, s24, v156
	v_add_u32_e32 v160, s25, v156
	v_add_u32_e32 v158, s24, v157
	v_add_u32_e32 v161, s24, v160
	v_add_u32_e32 v159, s24, v158
	v_add_u32_e32 v148, s24, v161
	s_nop 0
	v_add_u32_e32 v149, s24, v148
	v_cvt_pk_bf16_f32 v172, v126, v127
	v_cvt_pk_bf16_f32 v173, v128, v129
	v_cvt_pk_bf16_f32 v174, v122, v123
	v_cvt_pk_bf16_f32 v175, v124, v125
	global_store_dwordx4 v156, v[172:175], s[22:23]
	v_cvt_pk_bf16_f32 v176, v118, v119
	v_cvt_pk_bf16_f32 v177, v120, v121
	v_cvt_pk_bf16_f32 v178, v110, v111
	v_cvt_pk_bf16_f32 v179, v112, v113
	global_store_dwordx4 v156, v[176:179], s[22:23] offset:256
	v_cvt_pk_bf16_f32 v180, v114, v115
	v_cvt_pk_bf16_f32 v181, v116, v117
	v_cvt_pk_bf16_f32 v182, v106, v107
	v_cvt_pk_bf16_f32 v183, v108, v109
	global_store_dwordx4 v157, v[180:183], s[22:23]
	v_cvt_pk_bf16_f32 v184, v102, v103
	v_cvt_pk_bf16_f32 v185, v104, v105
	v_cvt_pk_bf16_f32 v186, v94, v95
	v_cvt_pk_bf16_f32 v187, v96, v97
	global_store_dwordx4 v157, v[184:187], s[22:23] offset:256
	v_cvt_pk_bf16_f32 v188, v98, v99
	v_cvt_pk_bf16_f32 v189, v100, v101
	v_cvt_pk_bf16_f32 v190, v90, v91
	v_cvt_pk_bf16_f32 v191, v92, v93
	global_store_dwordx4 v158, v[188:191], s[22:23]
	v_cvt_pk_bf16_f32 v192, v86, v87
	v_cvt_pk_bf16_f32 v193, v88, v89
	v_cvt_pk_bf16_f32 v194, v78, v79
	v_cvt_pk_bf16_f32 v195, v80, v81
	global_store_dwordx4 v158, v[192:195], s[22:23] offset:256
	v_cvt_pk_bf16_f32 v196, v82, v83
	v_cvt_pk_bf16_f32 v197, v84, v85
	v_cvt_pk_bf16_f32 v198, v74, v75
	v_cvt_pk_bf16_f32 v199, v76, v77
	global_store_dwordx4 v159, v[196:199], s[22:23]
	v_cvt_pk_bf16_f32 v200, v70, v71
	v_cvt_pk_bf16_f32 v201, v72, v73
	v_cvt_pk_bf16_f32 v202, v66, v67
	v_cvt_pk_bf16_f32 v203, v68, v69
	global_store_dwordx4 v159, v[200:203], s[22:23] offset:256
	v_cvt_pk_bf16_f32 v204, v62, v63
	v_cvt_pk_bf16_f32 v205, v64, v65
	v_cvt_pk_bf16_f32 v206, v58, v59
	v_cvt_pk_bf16_f32 v207, v60, v61
	global_store_dwordx4 v160, v[204:207], s[22:23]
	v_cvt_pk_bf16_f32 v208, v54, v55
	v_cvt_pk_bf16_f32 v209, v56, v57
	v_cvt_pk_bf16_f32 v210, v46, v47
	v_cvt_pk_bf16_f32 v211, v48, v49
	global_store_dwordx4 v160, v[208:211], s[22:23] offset:256
	v_cvt_pk_bf16_f32 v212, v50, v51
	v_cvt_pk_bf16_f32 v213, v52, v53
	v_cvt_pk_bf16_f32 v214, v42, v43
	v_cvt_pk_bf16_f32 v215, v44, v45
	global_store_dwordx4 v161, v[212:215], s[22:23]
	v_cvt_pk_bf16_f32 v216, v38, v39
	v_cvt_pk_bf16_f32 v217, v40, v41
	v_cvt_pk_bf16_f32 v218, v30, v31
	v_cvt_pk_bf16_f32 v219, v32, v33
	global_store_dwordx4 v161, v[216:219], s[22:23] offset:256
	v_cvt_pk_bf16_f32 v220, v34, v35
	v_cvt_pk_bf16_f32 v221, v36, v37
	v_cvt_pk_bf16_f32 v222, v26, v27
	v_cvt_pk_bf16_f32 v223, v28, v29
	global_store_dwordx4 v148, v[220:223], s[22:23]
	v_cvt_pk_bf16_f32 v224, v22, v23
	v_cvt_pk_bf16_f32 v225, v24, v25
	v_cvt_pk_bf16_f32 v226, v14, v15
	v_cvt_pk_bf16_f32 v227, v16, v17
	global_store_dwordx4 v148, v[224:227], s[22:23] offset:256
	v_cvt_pk_bf16_f32 v228, v18, v19
	v_cvt_pk_bf16_f32 v229, v20, v21
	v_cvt_pk_bf16_f32 v230, v10, v11
	v_cvt_pk_bf16_f32 v231, v12, v13
	global_store_dwordx4 v149, v[228:231], s[22:23]
	v_cvt_pk_bf16_f32 v236, v6, v7
	v_cvt_pk_bf16_f32 v237, v8, v9
	v_cvt_pk_bf16_f32 v238, v2, v3
	v_cvt_pk_bf16_f32 v239, v4, v5
	global_store_dwordx4 v149, v[236:239], s[22:23] offset:256
	s_andn2_b64 vcc, exec, s[4:5]
	s_mov_b64 s[4:5], -1
	s_cbranch_vccnz .LBB0_1639
	s_andn2_b64 vcc, exec, s[2:3]
	s_cbranch_vccnz .LBB0_1638
	s_barrier
	s_branch .LBB0_1638

; #define LAS __attribute__((address_space(3)))
; DI void attn_unit(const Args& A, LAS unsigned char* lds, int unit, int tid, int wave, int lane) {
;     ...
;     const int x = unit & 15; int r0 = unit >> 4; const int hh = r0 & 3; r0 >>= 2; const int b = r0 % NB, br = r0 / NB;
;     const int dil = br == 0 ? 1 : (br == 1 ? 4 : 16), lsub = SEQ / dil, nblk = lsub / 128;
;     const int res = x / nblk, nbk = x % nblk, l0 = nbk * 128, wbase = l0 - 64;
;     LAS bf16* Qs = (LAS bf16*)(lds + AT_QS); LAS bf16* Ks = (LAS bf16*)(lds + AT_KS); LAS bf16* Vt = (LAS bf16*)(lds + AT_VT); LAS float* btab = (LAS float*)(lds + AT_BT);
;     __syncthreads();
; #pragma unroll
;     for (int i = 0; i < 2; ++i) { const int id = tid + 512 * i, row = id >> 3, ch = id & 7; const int tok = b * SEQ + (l0 + row) * dil + res;
;         *(LAS u32x4_t*)(Qs + row * AT_QLD + ch * 8) = *(const u32x4_t*)(Z + (size_t)tok * ZLD + ZA + hh * 64 + ch * 8); }
;     for (int id = tid; id < 272 * 8; id += NTHR) { const int row = id >> 3, ch = id & 7; const int pos = wbase + row; u32x4_t v = (u32x4_t){0u, 0u, 0u, 0u};
;         if (row < 256 && pos >= 0 && pos < lsub) v = *(const u32x4_t*)(Z + (size_t)(b * SEQ + pos * dil + res) * ZLD + ZA + 256 + hh * 64 + ch * 8);
;         *(LAS u32x4_t*)(Ks + row * AT_QLD + ch * 8) = v; }
;     for (int id = tid; id < 272 * 8; id += NTHR) { const int key = id % 272, ch = id / 272; const int pos = wbase + key; u32x4_t v = (u32x4_t){0u, 0u, 0u, 0u};
;         if (key < 256 && pos >= 0 && pos < lsub) v = *(const u32x4_t*)(Z + (size_t)(b * SEQ + pos * dil + res) * ZLD + ZA + 512 + hh * 64 + ch * 8);
;         LAS bf16* d = Vt + (ch * 8) * AT_VLD + key;
;         d[0] = (bf16)(v.x & 0xffffu); d[AT_VLD] = (bf16)(v.x >> 16); d[2 * AT_VLD] = (bf16)(v.y & 0xffffu); d[3 * AT_VLD] = (bf16)(v.y >> 16);
;         d[4 * AT_VLD] = (bf16)(v.z & 0xffffu); d[5 * AT_VLD] = (bf16)(v.z >> 16); d[6 * AT_VLD] = (bf16)(v.w & 0xffffu); d[7 * AT_VLD] = (bf16)(v.w >> 16); }
;     if (tid < 129) btab[tid] = A.in[I_RELB][t5_bucket((tid - 64) * dil) * 4 + hh] * 1.4426950408889634f;
.LBB0_1704:
	s_cmp_lt_i32 s6, 14
	s_cselect_b64 s[0:1], -1, 0
	v_writelane_b32 v234, s0, 44
	s_nop 1
	v_writelane_b32 v234, s1, 45
	s_and_b64 s[0:1], s[0:1], s[2:3]
	s_andn2_b64 vcc, exec, s[0:1]
	s_cbranch_vccnz .LBB0_1958
	s_cmpk_gt_i32 s50, 0xa0
	s_cselect_b32 s0, 0x600, 0
	s_add_i32 s33, s0, s92
	s_cmpk_gt_i32 s33, 0x5ff
	s_mov_b32 s3, 0
	s_cbranch_scc1 .LBB0_1796
	s_mov_b32 s6, s33
	s_mov_b32 s7, s50
	s_movk_i32 s8, 0x600
	v_readlane_b32 s9, v235, 52
	v_readlane_b32 s2, v235, 9
	v_readlane_b32 s3, v235, 10
	v_readlane_b32 s4, v235, 19
	v_readlane_b32 s5, v235, 20
	s_mov_b32 s72, 0x3e38aa3b
	s_mov_b32 s73, 0x3e38aa3b
	v_lshrrev_b32_e32 v2, 3, v0
	v_and_b32_e32 v3, 7, v0
	v_lshlrev_b32_e32 v3, 4, v3
	s_movk_i32 s39, 0x90
	v_mad_u32_u24 v1, v2, s39, v3
	v_and_b32_e32 v5, 0xff, v0
	v_lshrrev_b32_e32 v6, 8, v0
	s_movk_i32 s39, 0x1180
	v_mul_u32_u24_e32 v4, s39, v6
	v_lshl_add_u32 v4, v5, 1, v4
	v_add_u32_e32 v4, 0xe100, v4
	v_lshlrev_b32_e32 v6, 4, v6
	v_lshlrev_b32_e32 v8, 2, v5
	v_add_u32_e32 v8, 0x16d00, v8
	v_subrev_u32_e32 v165, 16, v0
	s_movk_i32 s39, 0x81
	v_cmp_gt_u32_e64 s[42:43], s39, v165
	s_movk_i32 s39, 0xa0
	v_cmp_gt_u32_e64 s[48:49], s39, v0
	v_cmp_gt_u32_e64 s[46:47], 64, v0
	v_cmp_gt_u32_e64 s[44:45], 16, v146
	v_subrev_u32_e32 v165, 0x50, v0
	v_cmp_lt_i32_e32 vcc, 0, v165
	v_mov_b32_e32 v7, 0
	s_nop 0
	v_cndmask_b32_e64 v166, 0, 16, vcc
	v_lshlrev_b32_e32 v167, 0, v165
	v_sub_u32_e32 v168, 0, v167
	v_max_i32_e32 v167, v167, v168
	v_cvt_f32_u32_e32 v168, v167
	v_mul_f32_e32 v168, 0x3e000000, v168
	v_max_f32_e32 v168, 1.0, v168
	v_log_f32_e32 v168, v168
	v_cmp_gt_u32_e32 vcc, 8, v167
	v_mul_f32_e32 v168, 0x3f924925, v168
	v_cvt_i32_f32_e32 v168, v168
	v_min_i32_e32 v168, 7, v168
	v_add_u32_e32 v168, 8, v168
	v_cndmask_b32_e32 v168, v168, v167, vcc
	v_add_u32_e32 v168, v168, v166
	v_lshl_or_b32 v7, v168, 0, v7
	v_lshlrev_b32_e32 v167, 2, v165
	v_sub_u32_e32 v168, 0, v167
	v_max_i32_e32 v167, v167, v168
	v_cvt_f32_u32_e32 v168, v167
	v_mul_f32_e32 v168, 0x3e000000, v168
	v_max_f32_e32 v168, 1.0, v168
	v_log_f32_e32 v168, v168
	v_cmp_gt_u32_e32 vcc, 8, v167
	v_mul_f32_e32 v168, 0x3f924925, v168
	v_cvt_i32_f32_e32 v168, v168
	v_min_i32_e32 v168, 7, v168
	v_add_u32_e32 v168, 8, v168
	v_cndmask_b32_e32 v168, v168, v167, vcc
	v_add_u32_e32 v168, v168, v166
	v_lshl_or_b32 v7, v168, 8, v7
	v_lshlrev_b32_e32 v167, 4, v165
	v_sub_u32_e32 v168, 0, v167
	v_max_i32_e32 v167, v167, v168
	v_cvt_f32_u32_e32 v168, v167
	v_mul_f32_e32 v168, 0x3e000000, v168
	v_max_f32_e32 v168, 1.0, v168
	v_log_f32_e32 v168, v168
	v_cmp_gt_u32_e32 vcc, 8, v167
	v_mul_f32_e32 v168, 0x3f924925, v168
	v_cvt_i32_f32_e32 v168, v168
	v_min_i32_e32 v168, 7, v168
	v_add_u32_e32 v168, 8, v168
	v_cndmask_b32_e32 v168, v168, v167, vcc
	v_add_u32_e32 v168, v168, v166
	v_lshl_or_b32 v7, v168, 16, v7
	v_and_b32_e32 v165, 15, v146
	v_lshrrev_b32_e32 v166, 4, v146
	s_lshl_b32 s39, s9, 4
	v_add_u32_e32 v40, s39, v165
	s_movk_i32 s40, 0x90
	v_mul_u32_u24_e32 v34, s40, v40
	v_lshl_add_u32 v34, v166, 4, v34
	v_lshlrev_b32_e32 v167, 2, v166
	v_sub_u32_e32 v35, v167, v165
	v_lshlrev_b32_e32 v35, 2, v35
	v_add_u32_e32 v35, 0x16d40, v35
	v_add_u32_e32 v167, s39, v167
	v_lshlrev_b32_e32 v36, 2, v167
	v_add_u32_e32 v36, 0x16f80, v36
	s_movk_i32 s40, 0x230
	v_mul_u32_u24_e32 v37, s40, v165
	v_lshl_add_u32 v37, v167, 1, v37
	v_add_u32_e32 v37, 0xe100, v37
	v_add_u32_e32 v9, 0x2300, v37
	v_add_u32_e32 v118, 0x4600, v37
	v_add_u32_e32 v144, 0x6900, v37
	v_xor_b32_e32 v38, 16, v146
	v_lshlrev_b32_e32 v38, 2, v38
	v_xor_b32_e32 v39, 32, v146
	v_lshlrev_b32_e32 v39, 2, v39
	v_lshlrev_b32_e32 v41, 3, v166
	v_mov_b32_e32 v232, 0
	v_mov_b32_e32 v233, 0
	s_movk_i32 s40, 0x230
	v_mul_u32_u24_e32 v168, s40, v0
	v_add_u32_e32 v168, 0xe300, v168
	s_and_saveexec_b64 s[40:41], s[46:47]
	ds_write_b64 v168, v[232:233] offset:0
	ds_write_b64 v168, v[232:233] offset:8
	ds_write_b64 v168, v[232:233] offset:16
	ds_write_b64 v168, v[232:233] offset:24
	s_mov_b64 exec, s[40:41]
	s_and_b32 s39, s6, 15
	s_bfe_u32 s40, s6, 0x20004
	s_bfe_u32 s41, s6, 0x30006
	s_lshr_b32 s74, s6, 9
	s_lshl_b32 s75, s74, 1
	s_lshl_b32 s16, 1536, s75
	s_add_i32 s20, s75, 9
	s_add_i32 s26, s75, 4
	s_lshl_b32 s28, s74, 3
	s_lshr_b32 s29, 0x800, s75
	s_add_i32 s17, s29, -1
	s_sub_i32 s76, 4, s75
	s_lshr_b32 s77, s39, s76
	s_lshr_b32 s78, 16, s75
	s_add_i32 s78, s78, -1
	s_and_b32 s78, s39, s78
	s_lshl_b32 s19, s78, 7
	s_add_i32 s18, s19, 0xffffffc0
	s_lshl_b32 s79, s41, 11
	s_add_i32 s79, s79, s77
	s_lshl_b32 s80, s40, 7
	s_lshl_b32 s27, s40, 2
	s_mul_i32 s81, s79, 1536
	s_add_u32 s81, s81, s80
	s_add_u32 s81, s81, 0x28600000
	s_add_u32 s10, s2, s81
	s_addc_u32 s11, s3, 0
	s_lshl_b32 s82, s74, 14
	s_add_i32 s82, s82, s79
	s_lshl_b32 s83, s82, 9
	s_add_u32 s83, s83, s80
	s_add_u32 s83, s83, 0x34a00000
	s_add_u32 s12, s2, s83
	s_addc_u32 s13, s3, 0
	s_lshl_b32 s84, s82, 4
	s_add_u32 s84, s84, s27
	s_add_u32 s84, s84, 0x36200000
	s_add_u32 s14, s2, s84
	s_addc_u32 s15, s3, 0
	v_add_u32_e32 v165, s19, v2
	v_mad_u32_u24 v165, v165, s16, v3
	s_lshl_b32 s85, s16, 6
	global_load_dwordx4 v[120:123], v165, s[10:11]
	v_add_u32_e32 v166, s85, v165
	global_load_dwordx4 v[124:127], v166, s[10:11]
	v_add_u32_e32 v167, s18, v2
	v_med3_i32 v168, v167, 0, s17
	v_mad_u32_u24 v168, v168, s16, v3
	global_load_dwordx4 v[128:131], v168, s[10:11] offset:512
	v_add_u32_e32 v168, 64, v167
	v_med3_i32 v168, v168, 0, s17
	v_mad_u32_u24 v168, v168, s16, v3
	global_load_dwordx4 v[132:135], v168, s[10:11] offset:512
	v_add_u32_e32 v168, 0x80, v167
	v_med3_i32 v168, v168, 0, s17
	v_mad_u32_u24 v168, v168, s16, v3
	global_load_dwordx4 v[136:139], v168, s[10:11] offset:512
	v_add_u32_e32 v168, 0xc0, v167
	v_med3_i32 v168, v168, 0, s17
	v_mad_u32_u24 v168, v168, s16, v3
	global_load_dwordx4 v[140:143], v168, s[10:11] offset:512
	v_add_u32_e32 v169, s18, v5
	v_med3_i32 v169, v169, 0, s17
	v_mad_u32_u24 v169, v169, s16, v6
	global_load_dwordx4 v[148:151], v169, s[10:11] offset:1024
	global_load_dwordx4 v[152:155], v169, s[10:11] offset:1056
	global_load_dwordx4 v[156:159], v169, s[10:11] offset:1088
	global_load_dwordx4 v[160:163], v169, s[10:11] offset:1120
	v_bfe_u32 v171, v7, s28, 8
	v_lshl_add_u32 v171, v171, 4, s27
	s_mov_b64 exec, s[42:43]
	global_load_dword v164, v171, s[4:5]
	s_mov_b64 exec, -1

; DI void attn_unit(const Args& A, LAS unsigned char* lds, int unit, int tid, int wave, int lane) {
;     ...
;     const int x = unit & 15; int r0 = unit >> 4; const int hh = r0 & 3; r0 >>= 2; const int b = r0 % NB, br = r0 / NB;
;     const int dil = br == 0 ? 1 : (br == 1 ? 4 : 16), lsub = SEQ / dil, nblk = lsub / 128;
;     const int res = x / nblk, nbk = x % nblk, l0 = nbk * 128, wbase = l0 - 64;
;     LAS bf16* Qs = (LAS bf16*)(lds + AT_QS); LAS bf16* Ks = (LAS bf16*)(lds + AT_KS); LAS bf16* Vt = (LAS bf16*)(lds + AT_VT); LAS float* btab = (LAS float*)(lds + AT_BT);
;     __syncthreads();
; #pragma unroll
;     for (int i = 0; i < 2; ++i) { const int id = tid + 512 * i, row = id >> 3, ch = id & 7; const int tok = b * SEQ + (l0 + row) * dil + res;
;         *(LAS u32x4_t*)(Qs + row * AT_QLD + ch * 8) = *(const u32x4_t*)(Z + (size_t)tok * ZLD + ZA + hh * 64 + ch * 8); }
;     for (int id = tid; id < 272 * 8; id += NTHR) { const int row = id >> 3, ch = id & 7; const int pos = wbase + row; u32x4_t v = (u32x4_t){0u, 0u, 0u, 0u};
;         if (row < 256 && pos >= 0 && pos < lsub) v = *(const u32x4_t*)(Z + (size_t)(b * SEQ + pos * dil + res) * ZLD + ZA + 256 + hh * 64 + ch * 8);
;         *(LAS u32x4_t*)(Ks + row * AT_QLD + ch * 8) = v; }
;     for (int id = tid; id < 272 * 8; id += NTHR) { const int key = id % 272, ch = id / 272; const int pos = wbase + key; u32x4_t v = (u32x4_t){0u, 0u, 0u, 0u};
;         if (key < 256 && pos >= 0 && pos < lsub) v = *(const u32x4_t*)(Z + (size_t)(b * SEQ + pos * dil + res) * ZLD + ZA + 512 + hh * 64 + ch * 8);
;         LAS bf16* d = Vt + (ch * 8) * AT_VLD + key;
;         d[0] = (bf16)(v.x & 0xffffu); d[AT_VLD] = (bf16)(v.x >> 16); d[2 * AT_VLD] = (bf16)(v.y & 0xffffu); d[3 * AT_VLD] = (bf16)(v.y >> 16);
;         d[4 * AT_VLD] = (bf16)(v.z & 0xffffu); d[5 * AT_VLD] = (bf16)(v.z >> 16); d[6 * AT_VLD] = (bf16)(v.w & 0xffffu); d[7 * AT_VLD] = (bf16)(v.w >> 16); }
;     if (tid < 129) btab[tid] = A.in[I_RELB][t5_bucket((tid - 64) * dil) * 4 + hh] * 1.4426950408889634f;
; template <int l> DI void run_layer(const Args& A, LAS unsigned char* lds, const XcdBarrier& bar, int lo, int hi, int G, int bid, int tid, int lane, int wave, int gw, int ngw, int gtid, int nthr) {
;     ...
;     PH(3,
;           if (G > ATT_SCAN_BLK0 && bid >= ATT_SCAN_BLK0) phase_attn(A, lds, 0, ATT_UNITS - ATT_SPLIT, bid - ATT_SCAN_BLK0, G - ATT_SCAN_BLK0, tid, wave, lane);
.LBB0_2008:
	s_cmp_lt_i32 s6, 15
	s_cselect_b64 s[24:25], -1, 0
	s_and_b64 s[0:1], s[24:25], s[0:1]
	s_andn2_b64 vcc, exec, s[0:1]
	s_cbranch_vccnz .LBB0_2420
	s_cmpk_lt_i32 s50, 0xa1
	s_cselect_b64 s[0:1], -1, 0
	s_cmpk_lt_i32 s92, 0xa0
	s_cselect_b64 s[2:3], -1, 0
	s_or_b64 s[0:1], s[2:3], s[0:1]
	s_and_b64 vcc, exec, s[0:1]
	s_cbranch_vccnz .LBB0_2102
	s_add_i32 s33, s92, 0xffffff60
	s_cmpk_gt_u32 s33, 0x23f
	s_cbranch_scc1 .LBB0_2101
	s_mov_b32 s6, s33
	s_add_i32 s7, s50, 0xffffff60
	s_movk_i32 s8, 0x600
	v_readlane_b32 s9, v235, 52
	v_readlane_b32 s2, v235, 9
	v_readlane_b32 s3, v235, 10
	v_readlane_b32 s4, v235, 19
	v_readlane_b32 s5, v235, 20
	s_mov_b32 s72, 0x3e38aa3b
	s_mov_b32 s73, 0x3e38aa3b
	v_lshrrev_b32_e32 v2, 3, v0
	v_and_b32_e32 v3, 7, v0
	v_lshlrev_b32_e32 v3, 4, v3
	s_movk_i32 s39, 0x90
	v_mad_u32_u24 v1, v2, s39, v3
	v_and_b32_e32 v5, 0xff, v0
	v_lshrrev_b32_e32 v6, 8, v0
	s_movk_i32 s39, 0x1180
	v_mul_u32_u24_e32 v4, s39, v6
	v_lshl_add_u32 v4, v5, 1, v4
	v_add_u32_e32 v4, 0xe100, v4
	v_lshlrev_b32_e32 v6, 4, v6
	v_lshlrev_b32_e32 v8, 2, v5
	v_add_u32_e32 v8, 0x16d00, v8
	v_subrev_u32_e32 v165, 16, v0
	s_movk_i32 s39, 0x81
	v_cmp_gt_u32_e64 s[42:43], s39, v165
	s_movk_i32 s39, 0xa0
	v_cmp_gt_u32_e64 s[48:49], s39, v0
	v_cmp_gt_u32_e64 s[46:47], 64, v0
	v_cmp_gt_u32_e64 s[44:45], 16, v146
	v_subrev_u32_e32 v165, 0x50, v0
	v_cmp_lt_i32_e32 vcc, 0, v165
	v_mov_b32_e32 v7, 0
	s_nop 0
	v_cndmask_b32_e64 v166, 0, 16, vcc
	v_lshlrev_b32_e32 v167, 0, v165
	v_sub_u32_e32 v168, 0, v167
	v_max_i32_e32 v167, v167, v168
	v_cvt_f32_u32_e32 v168, v167
	v_mul_f32_e32 v168, 0x3e000000, v168
	v_max_f32_e32 v168, 1.0, v168
	v_log_f32_e32 v168, v168
	v_cmp_gt_u32_e32 vcc, 8, v167
	v_mul_f32_e32 v168, 0x3f924925, v168
	v_cvt_i32_f32_e32 v168, v168
	v_min_i32_e32 v168, 7, v168
	v_add_u32_e32 v168, 8, v168
	v_cndmask_b32_e32 v168, v168, v167, vcc
	v_add_u32_e32 v168, v168, v166
	v_lshl_or_b32 v7, v168, 0, v7
	v_lshlrev_b32_e32 v167, 2, v165
	v_sub_u32_e32 v168, 0, v167
	v_max_i32_e32 v167, v167, v168
	v_cvt_f32_u32_e32 v168, v167
	v_mul_f32_e32 v168, 0x3e000000, v168
	v_max_f32_e32 v168, 1.0, v168
	v_log_f32_e32 v168, v168
	v_cmp_gt_u32_e32 vcc, 8, v167
	v_mul_f32_e32 v168, 0x3f924925, v168
	v_cvt_i32_f32_e32 v168, v168
	v_min_i32_e32 v168, 7, v168
	v_add_u32_e32 v168, 8, v168
	v_cndmask_b32_e32 v168, v168, v167, vcc
	v_add_u32_e32 v168, v168, v166
	v_lshl_or_b32 v7, v168, 8, v7
	v_lshlrev_b32_e32 v167, 4, v165
	v_sub_u32_e32 v168, 0, v167
	v_max_i32_e32 v167, v167, v168
	v_cvt_f32_u32_e32 v168, v167
	v_mul_f32_e32 v168, 0x3e000000, v168
	v_max_f32_e32 v168, 1.0, v168
	v_log_f32_e32 v168, v168
	v_cmp_gt_u32_e32 vcc, 8, v167
	v_mul_f32_e32 v168, 0x3f924925, v168
	v_cvt_i32_f32_e32 v168, v168
	v_min_i32_e32 v168, 7, v168
	v_add_u32_e32 v168, 8, v168
	v_cndmask_b32_e32 v168, v168, v167, vcc
	v_add_u32_e32 v168, v168, v166
	v_lshl_or_b32 v7, v168, 16, v7
	v_and_b32_e32 v165, 15, v146
	v_lshrrev_b32_e32 v166, 4, v146
	s_lshl_b32 s39, s9, 4
	v_add_u32_e32 v40, s39, v165
	s_movk_i32 s40, 0x90
	v_mul_u32_u24_e32 v34, s40, v40
	v_lshl_add_u32 v34, v166, 4, v34
	v_lshlrev_b32_e32 v167, 2, v166
	v_sub_u32_e32 v35, v167, v165
	v_lshlrev_b32_e32 v35, 2, v35
	v_add_u32_e32 v35, 0x16d40, v35
	v_add_u32_e32 v167, s39, v167
	v_lshlrev_b32_e32 v36, 2, v167
	v_add_u32_e32 v36, 0x16f80, v36
	s_movk_i32 s40, 0x230
	v_mul_u32_u24_e32 v37, s40, v165
	v_lshl_add_u32 v37, v167, 1, v37
	v_add_u32_e32 v37, 0xe100, v37
	v_add_u32_e32 v9, 0x2300, v37
	v_add_u32_e32 v118, 0x4600, v37
	v_add_u32_e32 v144, 0x6900, v37
	v_xor_b32_e32 v38, 16, v146
	v_lshlrev_b32_e32 v38, 2, v38
	v_xor_b32_e32 v39, 32, v146
	v_lshlrev_b32_e32 v39, 2, v39
	v_lshlrev_b32_e32 v41, 3, v166
	v_mov_b32_e32 v232, 0
	v_mov_b32_e32 v233, 0
	s_movk_i32 s40, 0x230
	v_mul_u32_u24_e32 v168, s40, v0
	v_add_u32_e32 v168, 0xe300, v168
	s_and_saveexec_b64 s[40:41], s[46:47]
	ds_write_b64 v168, v[232:233] offset:0
	ds_write_b64 v168, v[232:233] offset:8
	ds_write_b64 v168, v[232:233] offset:16
	ds_write_b64 v168, v[232:233] offset:24
	s_mov_b64 exec, s[40:41]
	s_and_b32 s39, s6, 15
	s_bfe_u32 s40, s6, 0x20004
	s_bfe_u32 s41, s6, 0x30006
	s_lshr_b32 s74, s6, 9
	s_lshl_b32 s75, s74, 1
	s_lshl_b32 s16, 1536, s75
	s_add_i32 s20, s75, 9
	s_add_i32 s26, s75, 4
	s_lshl_b32 s28, s74, 3
	s_lshr_b32 s29, 0x800, s75
	s_add_i32 s17, s29, -1
	s_sub_i32 s76, 4, s75
	s_lshr_b32 s77, s39, s76
	s_lshr_b32 s78, 16, s75
	s_add_i32 s78, s78, -1
	s_and_b32 s78, s39, s78
	s_lshl_b32 s19, s78, 7
	s_add_i32 s18, s19, 0xffffffc0
	s_lshl_b32 s79, s41, 11
	s_add_i32 s79, s79, s77
	s_lshl_b32 s80, s40, 7
	s_lshl_b32 s27, s40, 2
	s_mul_i32 s81, s79, 1536
	s_add_u32 s81, s81, s80
	s_add_u32 s81, s81, 0x28600000
	s_add_u32 s10, s2, s81
	s_addc_u32 s11, s3, 0
	s_lshl_b32 s82, s74, 14
	s_add_i32 s82, s82, s79
	s_lshl_b32 s83, s82, 9
	s_add_u32 s83, s83, s80
	s_add_u32 s83, s83, 0x34a00000
	s_add_u32 s12, s2, s83
	s_addc_u32 s13, s3, 0
	s_lshl_b32 s84, s82, 4
	s_add_u32 s84, s84, s27
	s_add_u32 s84, s84, 0x36200000
	s_add_u32 s14, s2, s84
	s_addc_u32 s15, s3, 0
	v_add_u32_e32 v165, s19, v2
	v_mad_u32_u24 v165, v165, s16, v3
	s_lshl_b32 s85, s16, 6
	global_load_dwordx4 v[120:123], v165, s[10:11]
	v_add_u32_e32 v166, s85, v165
	global_load_dwordx4 v[124:127], v166, s[10:11]
	v_add_u32_e32 v167, s18, v2
	v_med3_i32 v168, v167, 0, s17
	v_mad_u32_u24 v168, v168, s16, v3
	global_load_dwordx4 v[128:131], v168, s[10:11] offset:512
	v_add_u32_e32 v168, 64, v167
	v_med3_i32 v168, v168, 0, s17
	v_mad_u32_u24 v168, v168, s16, v3
	global_load_dwordx4 v[132:135], v168, s[10:11] offset:512
	v_add_u32_e32 v168, 0x80, v167
	v_med3_i32 v168, v168, 0, s17
	v_mad_u32_u24 v168, v168, s16, v3
	global_load_dwordx4 v[136:139], v168, s[10:11] offset:512
	v_add_u32_e32 v168, 0xc0, v167
	v_med3_i32 v168, v168, 0, s17
	v_mad_u32_u24 v168, v168, s16, v3
	global_load_dwordx4 v[140:143], v168, s[10:11] offset:512
	v_add_u32_e32 v169, s18, v5
	v_med3_i32 v169, v169, 0, s17
	v_mad_u32_u24 v169, v169, s16, v6
	global_load_dwordx4 v[148:151], v169, s[10:11] offset:1024
	global_load_dwordx4 v[152:155], v169, s[10:11] offset:1056
	global_load_dwordx4 v[156:159], v169, s[10:11] offset:1088
	global_load_dwordx4 v[160:163], v169, s[10:11] offset:1120
	v_bfe_u32 v171, v7, s28, 8
	v_lshl_add_u32 v171, v171, 4, s27
	s_mov_b64 exec, s[42:43]
	global_load_dword v164, v171, s[4:5]
	s_mov_b64 exec, -1

; __device__ __forceinline__ unsigned xb_add(unsigned* p, unsigned v) { return __hip_atomic_fetch_add(p, v, __ATOMIC_RELAXED, __HIP_MEMORY_SCOPE_AGENT); }
; __device__ __forceinline__ void xcd_barrier(const XcdBarrier& b) {
;     asm volatile("s_waitcnt vmcnt(0)" ::: "memory");
;     __syncthreads();
;     if (threadIdx.x == 0) {
;         unsigned* bar = b.bar;
;         __builtin_amdgcn_s_waitcnt(0);
;         unsigned nloc = b.st[0], nx = b.st[1];
;         if (nloc == 0u) { xcd_barrier_complete(bar, b.x, nloc, nx); b.st[0] = nloc; b.st[1] = nx; }
;         const unsigned old = xb_add(&bar[XB_XSUB(b.x)], 1u);
; template <int l> DI void run_layer(const Args& A, LAS unsigned char* lds, const XcdBarrier& bar, int lo, int hi, int G, int bid, int tid, int lane, int wave, int gw, int ngw, int gtid, int nthr) {
;     ...
;           for (int rep = 0; rep < 1 + ((MK_DUP >> 14) & 1); ++rep) for (int u = bid; u < 96; u += G) rwkv_r2_unit(A, lds, u, tid, wave, lane);
;           for (int rep = 0; rep < 1 + ((MK_DUP >> 15) & 1); ++rep) for (int u = bid; u < 96 + 64; u += G) { if (u >= 96) mlstm_m2_unit(A, lds, u - 96, tid, wave, lane); });
.Lm21_unext:
	s_add_i32 s6, s6, s50
	s_branch .Lm21_uloop
.LBB0_2420:
	v_readlane_b32 s4, v235, 9
	v_readlane_b32 s7, v235, 12
	s_cmp_gt_i32 s7, 15
	s_cselect_b64 s[0:1], -1, 0
	s_and_b64 s[2:3], s[24:25], s[0:1]
	v_readlane_b32 s5, v235, 10
	v_readlane_b32 s6, v235, 11
	s_andn2_b64 vcc, exec, s[2:3]
	s_cbranch_vccnz .LBB0_2470
	s_waitcnt vmcnt(0)
	v_cmp_eq_u32_e32 vcc, 0, v0
	s_waitcnt vmcnt(0) lgkmcnt(0)
	s_barrier
	s_and_saveexec_b64 s[2:3], vcc
	s_cbranch_execz .LBB0_2469
	s_add_i32 s4, 0, 0x23f20
	v_mov_b32_e32 v1, s4
	s_waitcnt vmcnt(0) expcnt(0) lgkmcnt(0)
	ds_read_b32 v3, v1
	s_add_i32 s4, 0, 0x23f24
	v_mov_b32_e32 v1, s4
	ds_read_b32 v1, v1
	s_waitcnt lgkmcnt(1)
	v_cmp_ne_u32_e32 vcc, 0, v3
	s_cbranch_vccnz .LBB0_2437
	v_readlane_b32 s4, v235, 13
	v_readlane_b32 s5, v235, 14
	s_load_dwordx2 s[8:9], s[4:5], 0x4
	v_readlane_b32 s40, v235, 9
	v_readlane_b32 s41, v235, 10
	s_add_u32 s4, s40, 0x4200
	s_addc_u32 s5, s41, 0
	s_add_u32 s6, s40, 0x4400
	s_addc_u32 s7, s41, 0
	s_waitcnt lgkmcnt(0)
	s_mul_i32 s33, s8, s50
	s_add_u32 s8, s40, 0x4500
	s_mul_i32 s33, s33, s9
	s_addc_u32 s9, s41, 0
	s_add_u32 s10, s40, 0x4600
	s_addc_u32 s11, s41, 0
	s_add_u32 s12, s40, 0x4700
	s_addc_u32 s13, s41, 0
	s_add_u32 s14, s40, 0x4800
	s_addc_u32 s15, s41, 0
	s_add_u32 s16, s40, 0x4900
	s_addc_u32 s17, s41, 0
	s_add_u32 s18, s40, 0x4a00
	s_addc_u32 s19, s41, 0
	s_add_u32 s20, s40, 0x4b00
	s_addc_u32 s21, s41, 0
	s_add_u32 s22, s40, 0x4c00
	s_addc_u32 s23, s41, 0
	s_add_u32 s24, s40, 0x4d00
	s_addc_u32 s25, s41, 0
	s_add_u32 s26, s40, 0x4e00
	s_addc_u32 s27, s41, 0
	s_add_u32 s28, s40, 0x4f00
	s_addc_u32 s29, s41, 0
	s_add_u32 s30, s40, 0x5000
	s_addc_u32 s31, s41, 0
	s_add_u32 s34, s40, 0x5100
	s_addc_u32 s35, s41, 0
	s_add_u32 s36, s40, 0x5200
	s_addc_u32 s37, s41, 0
	s_add_u32 s38, s40, 0x5300
	s_addc_u32 s39, s41, 0
	s_mov_b32 s46, 1
	v_mov_b32_e32 v17, 0
	v_readlane_b32 s42, v235, 11
	v_readlane_b32 s43, v235, 12
	s_branch .LBB0_2425
